# speedup vs baseline: 1.0012x; 1.0012x over previous
.LBB1_82:
	ds_read_b128 v[130:133], v219 offset:32768
	ds_read_b128 v[134:137], v219 offset:33792
	ds_read_b128 v[138:141], v219 offset:34816
	ds_read_b128 v[142:145], v219 offset:35840
	ds_read_b128 v[178:181], v219 offset:49152
	ds_read_b128 v[182:185], v219 offset:50176
	ds_read_b128 v[186:189], v219 offset:51200
	ds_read_b128 v[190:193], v219 offset:52224
	ds_read_b128 v[146:149], v220
	ds_read_b128 v[150:153], v220 offset:1024
	ds_read_b128 v[154:157], v221
	ds_read_b128 v[158:161], v221 offset:1024
	ds_read_b128 v[162:165], v222
	ds_read_b128 v[166:169], v222 offset:1024
	ds_read_b128 v[170:173], v223
	ds_read_b128 v[174:177], v223 offset:1024
	s_add_i32 s12, s8, 1
	v_readlane_b32 s9, v248, s12
	s_mov_b32 m0, s43
	s_nop 1
	v_add_u32_e32 v251, s9, v249
	global_load_lds_dwordx4 v251, s[18:19]
	v_add_u32_e32 v251, s9, v250
	s_mov_b32 m0, s44
	s_nop 0
	global_load_lds_dwordx4 v251, s[18:19]
	s_waitcnt vmcnt(8) lgkmcnt(0)
	s_barrier
	s_setprio 1
	v_mfma_f32_16x16x32_f16 v[124:127], v[130:133], v[146:149], v[124:127]
	v_mfma_f32_16x16x32_f16 v[120:123], v[138:141], v[146:149], v[120:123]
	v_mfma_f32_16x16x32_f16 v[116:119], v[130:133], v[154:157], v[116:119]
	v_mfma_f32_16x16x32_f16 v[112:115], v[138:141], v[154:157], v[112:115]
	v_mfma_f32_16x16x32_f16 v[108:111], v[130:133], v[162:165], v[108:111]
	v_mfma_f32_16x16x32_f16 v[104:107], v[138:141], v[162:165], v[104:107]
	v_mfma_f32_16x16x32_f16 v[100:103], v[130:133], v[170:173], v[100:103]
	v_mfma_f32_16x16x32_f16 v[96:99], v[138:141], v[170:173], v[96:99]
	v_mfma_f32_16x16x32_f16 v[124:127], v[134:137], v[150:153], v[124:127]
	v_mfma_f32_16x16x32_f16 v[120:123], v[142:145], v[150:153], v[120:123]
	v_mfma_f32_16x16x32_f16 v[116:119], v[134:137], v[158:161], v[116:119]
	v_mfma_f32_16x16x32_f16 v[112:115], v[142:145], v[158:161], v[112:115]
	v_mfma_f32_16x16x32_f16 v[108:111], v[134:137], v[166:169], v[108:111]
	v_mfma_f32_16x16x32_f16 v[104:107], v[142:145], v[166:169], v[104:107]
	v_mfma_f32_16x16x32_f16 v[100:103], v[134:137], v[174:177], v[100:103]
	v_mfma_f32_16x16x32_f16 v[96:99], v[142:145], v[174:177], v[96:99]
	v_mfma_f32_16x16x32_f16 v[52:55], v[178:181], v[146:149], v[52:55]
	v_mfma_f32_16x16x32_f16 v[40:43], v[186:189], v[146:149], v[40:43]
	v_mfma_f32_16x16x32_f16 v[36:39], v[178:181], v[154:157], v[36:39]
	v_mfma_f32_16x16x32_f16 v[32:35], v[186:189], v[154:157], v[32:35]
	v_mfma_f32_16x16x32_f16 v[28:31], v[178:181], v[162:165], v[28:31]
	v_mfma_f32_16x16x32_f16 v[24:27], v[186:189], v[162:165], v[24:27]
	v_mfma_f32_16x16x32_f16 v[20:23], v[178:181], v[170:173], v[20:23]
	v_mfma_f32_16x16x32_f16 v[16:19], v[186:189], v[170:173], v[16:19]
	v_mfma_f32_16x16x32_f16 v[52:55], v[182:185], v[150:153], v[52:55]
	v_mfma_f32_16x16x32_f16 v[40:43], v[190:193], v[150:153], v[40:43]
	v_mfma_f32_16x16x32_f16 v[36:39], v[182:185], v[158:161], v[36:39]
	v_mfma_f32_16x16x32_f16 v[32:35], v[190:193], v[158:161], v[32:35]
	v_mfma_f32_16x16x32_f16 v[28:31], v[182:185], v[166:169], v[28:31]
	v_mfma_f32_16x16x32_f16 v[24:27], v[190:193], v[166:169], v[24:27]
	v_mfma_f32_16x16x32_f16 v[20:23], v[182:185], v[174:177], v[20:23]
	v_mfma_f32_16x16x32_f16 v[16:19], v[190:193], v[174:177], v[16:19]
	s_setprio 0
	s_barrier
	ds_read_b128 v[146:149], v220 offset:16384
	ds_read_b128 v[150:153], v220 offset:17408
	ds_read_b128 v[154:157], v221 offset:16384
	ds_read_b128 v[158:161], v221 offset:17408
	ds_read_b128 v[162:165], v222 offset:16384
	ds_read_b128 v[166:169], v222 offset:17408
	ds_read_b128 v[170:173], v223 offset:16384
	ds_read_b128 v[174:177], v223 offset:17408
	v_add_u32_e32 v129, s7, v128
	s_mov_b32 m0, s22
	v_add_u32_e32 v194, 0xffffff80, v129
	global_load_lds_dwordx4 v194, s[10:11]
	v_add_u32_e32 v194, 0x47f80, v129
	s_mov_b32 m0, s23
	s_add_i32 s9, s8, 2
	global_load_lds_dwordx4 v194, s[10:11]
	v_readlane_b32 s13, v248, s9
	s_mov_b32 m0, s21
	s_nop 1
	v_add_u32_e32 v194, s13, v206
	global_load_lds_dwordx4 v194, s[18:19]
	v_add_u32_e32 v194, s13, v213
	s_mov_b32 m0, s24
	s_nop 0
	global_load_lds_dwordx4 v194, s[18:19]
	s_mov_b32 m0, s25
	v_add_u32_e32 v194, 0x8ff80, v129
	global_load_lds_dwordx4 v194, s[10:11]
	v_add_u32_e32 v194, 0xd7f80, v129
	s_mov_b32 m0, s26
	s_nop 0
	global_load_lds_dwordx4 v194, s[10:11]
	s_waitcnt vmcnt(8) lgkmcnt(0)
	s_barrier
	s_setprio 1
	v_mfma_f32_16x16x32_f16 v[12:15], v[130:133], v[146:149], v[12:15]
	v_mfma_f32_16x16x32_f16 v[8:11], v[138:141], v[146:149], v[8:11]
	v_mfma_f32_16x16x32_f16 v[4:7], v[130:133], v[154:157], v[4:7]
	v_mfma_f32_16x16x32_f16 v[0:3], v[138:141], v[154:157], v[0:3]
	v_mfma_f32_16x16x32_f16 v[44:47], v[130:133], v[162:165], v[44:47]
	v_mfma_f32_16x16x32_f16 v[48:51], v[138:141], v[162:165], v[48:51]
	v_mfma_f32_16x16x32_f16 v[56:59], v[130:133], v[170:173], v[56:59]
	v_mfma_f32_16x16x32_f16 v[60:63], v[138:141], v[170:173], v[60:63]
	v_mfma_f32_16x16x32_f16 v[12:15], v[134:137], v[150:153], v[12:15]
	v_mfma_f32_16x16x32_f16 v[8:11], v[142:145], v[150:153], v[8:11]
	v_mfma_f32_16x16x32_f16 v[4:7], v[134:137], v[158:161], v[4:7]
	v_mfma_f32_16x16x32_f16 v[0:3], v[142:145], v[158:161], v[0:3]
	v_mfma_f32_16x16x32_f16 v[44:47], v[134:137], v[166:169], v[44:47]
	v_mfma_f32_16x16x32_f16 v[48:51], v[142:145], v[166:169], v[48:51]
	v_mfma_f32_16x16x32_f16 v[56:59], v[134:137], v[174:177], v[56:59]
	v_mfma_f32_16x16x32_f16 v[60:63], v[142:145], v[174:177], v[60:63]
	v_mfma_f32_16x16x32_f16 v[64:67], v[178:181], v[146:149], v[64:67]
	v_mfma_f32_16x16x32_f16 v[68:71], v[186:189], v[146:149], v[68:71]
	v_mfma_f32_16x16x32_f16 v[72:75], v[178:181], v[154:157], v[72:75]
	v_mfma_f32_16x16x32_f16 v[76:79], v[186:189], v[154:157], v[76:79]
	v_mfma_f32_16x16x32_f16 v[80:83], v[178:181], v[162:165], v[80:83]
	v_mfma_f32_16x16x32_f16 v[84:87], v[186:189], v[162:165], v[84:87]
	v_mfma_f32_16x16x32_f16 v[88:91], v[178:181], v[170:173], v[88:91]
	v_mfma_f32_16x16x32_f16 v[92:95], v[186:189], v[170:173], v[92:95]
	v_mfma_f32_16x16x32_f16 v[64:67], v[182:185], v[150:153], v[64:67]
	v_mfma_f32_16x16x32_f16 v[68:71], v[190:193], v[150:153], v[68:71]
	v_mfma_f32_16x16x32_f16 v[72:75], v[182:185], v[158:161], v[72:75]
	v_mfma_f32_16x16x32_f16 v[76:79], v[190:193], v[158:161], v[76:79]
	v_mfma_f32_16x16x32_f16 v[80:83], v[182:185], v[166:169], v[80:83]
	v_mfma_f32_16x16x32_f16 v[84:87], v[190:193], v[166:169], v[84:87]
	v_mfma_f32_16x16x32_f16 v[88:91], v[182:185], v[174:177], v[88:91]
	v_mfma_f32_16x16x32_f16 v[92:95], v[190:193], v[174:177], v[92:95]
	s_setprio 0
	s_barrier
	ds_read_b128 v[130:133], v224
	ds_read_b128 v[134:137], v224 offset:1024
	ds_read_b128 v[138:141], v224 offset:2048
	ds_read_b128 v[142:145], v224 offset:3072
	ds_read_b128 v[178:181], v229
	ds_read_b128 v[182:185], v229 offset:1024
	ds_read_b128 v[186:189], v229 offset:2048
	ds_read_b128 v[190:193], v229 offset:3072
	ds_read_b128 v[146:149], v225
	ds_read_b128 v[150:153], v225 offset:1024
	ds_read_b128 v[154:157], v226
	ds_read_b128 v[158:161], v226 offset:1024
	ds_read_b128 v[162:165], v227
	ds_read_b128 v[166:169], v227 offset:1024
	ds_read_b128 v[170:173], v228
	ds_read_b128 v[174:177], v228 offset:1024
	v_readlane_b32 s12, v248, s9
	s_mov_b32 m0, s27
	s_nop 1
	v_add_u32_e32 v251, s12, v249
	global_load_lds_dwordx4 v251, s[18:19]
	v_add_u32_e32 v251, s12, v250
	s_mov_b32 m0, s28
	s_nop 0
	global_load_lds_dwordx4 v251, s[18:19]
	s_waitcnt vmcnt(8) lgkmcnt(0)
	s_barrier
	s_setprio 1
	v_mfma_f32_16x16x32_f16 v[124:127], v[130:133], v[146:149], v[124:127]
	v_mfma_f32_16x16x32_f16 v[120:123], v[138:141], v[146:149], v[120:123]
	v_mfma_f32_16x16x32_f16 v[116:119], v[130:133], v[154:157], v[116:119]
	v_mfma_f32_16x16x32_f16 v[112:115], v[138:141], v[154:157], v[112:115]
	v_mfma_f32_16x16x32_f16 v[108:111], v[130:133], v[162:165], v[108:111]
	v_mfma_f32_16x16x32_f16 v[104:107], v[138:141], v[162:165], v[104:107]
	v_mfma_f32_16x16x32_f16 v[100:103], v[130:133], v[170:173], v[100:103]
	v_mfma_f32_16x16x32_f16 v[96:99], v[138:141], v[170:173], v[96:99]
	v_mfma_f32_16x16x32_f16 v[124:127], v[134:137], v[150:153], v[124:127]
	v_mfma_f32_16x16x32_f16 v[120:123], v[142:145], v[150:153], v[120:123]
	v_mfma_f32_16x16x32_f16 v[116:119], v[134:137], v[158:161], v[116:119]
	v_mfma_f32_16x16x32_f16 v[112:115], v[142:145], v[158:161], v[112:115]
	v_mfma_f32_16x16x32_f16 v[108:111], v[134:137], v[166:169], v[108:111]
	v_mfma_f32_16x16x32_f16 v[104:107], v[142:145], v[166:169], v[104:107]
	v_mfma_f32_16x16x32_f16 v[100:103], v[134:137], v[174:177], v[100:103]
	v_mfma_f32_16x16x32_f16 v[96:99], v[142:145], v[174:177], v[96:99]
	v_mfma_f32_16x16x32_f16 v[52:55], v[178:181], v[146:149], v[52:55]
	v_mfma_f32_16x16x32_f16 v[40:43], v[186:189], v[146:149], v[40:43]
	v_mfma_f32_16x16x32_f16 v[36:39], v[178:181], v[154:157], v[36:39]
	v_mfma_f32_16x16x32_f16 v[32:35], v[186:189], v[154:157], v[32:35]
	v_mfma_f32_16x16x32_f16 v[28:31], v[178:181], v[162:165], v[28:31]
	v_mfma_f32_16x16x32_f16 v[24:27], v[186:189], v[162:165], v[24:27]
	v_mfma_f32_16x16x32_f16 v[20:23], v[178:181], v[170:173], v[20:23]
	v_mfma_f32_16x16x32_f16 v[16:19], v[186:189], v[170:173], v[16:19]
	v_mfma_f32_16x16x32_f16 v[52:55], v[182:185], v[150:153], v[52:55]
	v_mfma_f32_16x16x32_f16 v[40:43], v[190:193], v[150:153], v[40:43]
	v_mfma_f32_16x16x32_f16 v[36:39], v[182:185], v[158:161], v[36:39]
	v_mfma_f32_16x16x32_f16 v[32:35], v[190:193], v[158:161], v[32:35]
	v_mfma_f32_16x16x32_f16 v[28:31], v[182:185], v[166:169], v[28:31]
	v_mfma_f32_16x16x32_f16 v[24:27], v[190:193], v[166:169], v[24:27]
	v_mfma_f32_16x16x32_f16 v[20:23], v[182:185], v[174:177], v[20:23]
	v_mfma_f32_16x16x32_f16 v[16:19], v[190:193], v[174:177], v[16:19]
	s_setprio 0
	s_barrier
	ds_read_b128 v[146:149], v230
	ds_read_b128 v[150:153], v230 offset:1024
	ds_read_b128 v[154:157], v231
	ds_read_b128 v[158:161], v231 offset:1024
	ds_read_b128 v[162:165], v232
	ds_read_b128 v[166:169], v232 offset:1024
	ds_read_b128 v[170:173], v233
	ds_read_b128 v[174:177], v233 offset:1024
	s_mov_b32 m0, s37
	v_add_u32_e32 v194, 0x48000, v129
	global_load_lds_dwordx4 v129, s[10:11]
	s_mov_b32 m0, s38
	s_add_i32 s12, s8, 3
	global_load_lds_dwordx4 v194, s[10:11]
	v_readlane_b32 s13, v248, s12
	s_mov_b32 m0, s39
	s_nop 1
	v_add_u32_e32 v194, s13, v206
	global_load_lds_dwordx4 v194, s[18:19]
	v_add_u32_e32 v194, s13, v213
	s_mov_b32 m0, s40
	s_nop 0
	global_load_lds_dwordx4 v194, s[18:19]
	s_mov_b32 m0, s41
	v_add_u32_e32 v194, 0x90000, v129
	global_load_lds_dwordx4 v194, s[10:11]
	v_add_u32_e32 v194, 0xd8000, v129
	s_mov_b32 m0, s42
	s_nop 0
	global_load_lds_dwordx4 v194, s[10:11]
	s_waitcnt vmcnt(8) lgkmcnt(0)
	s_barrier
	s_setprio 1
	v_mfma_f32_16x16x32_f16 v[12:15], v[130:133], v[146:149], v[12:15]
	v_mfma_f32_16x16x32_f16 v[8:11], v[138:141], v[146:149], v[8:11]
	v_mfma_f32_16x16x32_f16 v[4:7], v[130:133], v[154:157], v[4:7]
	v_mfma_f32_16x16x32_f16 v[0:3], v[138:141], v[154:157], v[0:3]
	v_mfma_f32_16x16x32_f16 v[44:47], v[130:133], v[162:165], v[44:47]
	v_mfma_f32_16x16x32_f16 v[48:51], v[138:141], v[162:165], v[48:51]
	v_mfma_f32_16x16x32_f16 v[56:59], v[130:133], v[170:173], v[56:59]
	v_mfma_f32_16x16x32_f16 v[60:63], v[138:141], v[170:173], v[60:63]
	v_mfma_f32_16x16x32_f16 v[12:15], v[134:137], v[150:153], v[12:15]
	v_mfma_f32_16x16x32_f16 v[8:11], v[142:145], v[150:153], v[8:11]
	v_mfma_f32_16x16x32_f16 v[4:7], v[134:137], v[158:161], v[4:7]
	v_mfma_f32_16x16x32_f16 v[0:3], v[142:145], v[158:161], v[0:3]
	v_mfma_f32_16x16x32_f16 v[44:47], v[134:137], v[166:169], v[44:47]
	v_mfma_f32_16x16x32_f16 v[48:51], v[142:145], v[166:169], v[48:51]
	v_mfma_f32_16x16x32_f16 v[56:59], v[134:137], v[174:177], v[56:59]
	v_mfma_f32_16x16x32_f16 v[60:63], v[142:145], v[174:177], v[60:63]
	v_mfma_f32_16x16x32_f16 v[64:67], v[178:181], v[146:149], v[64:67]
	v_mfma_f32_16x16x32_f16 v[68:71], v[186:189], v[146:149], v[68:71]
	v_mfma_f32_16x16x32_f16 v[72:75], v[178:181], v[154:157], v[72:75]
	v_mfma_f32_16x16x32_f16 v[76:79], v[186:189], v[154:157], v[76:79]
	v_mfma_f32_16x16x32_f16 v[80:83], v[178:181], v[162:165], v[80:83]
	v_mfma_f32_16x16x32_f16 v[84:87], v[186:189], v[162:165], v[84:87]
	v_mfma_f32_16x16x32_f16 v[88:91], v[178:181], v[170:173], v[88:91]
	v_mfma_f32_16x16x32_f16 v[92:95], v[186:189], v[170:173], v[92:95]
	v_mfma_f32_16x16x32_f16 v[64:67], v[182:185], v[150:153], v[64:67]
	v_mfma_f32_16x16x32_f16 v[68:71], v[190:193], v[150:153], v[68:71]
	v_mfma_f32_16x16x32_f16 v[72:75], v[182:185], v[158:161], v[72:75]
	v_mfma_f32_16x16x32_f16 v[76:79], v[190:193], v[158:161], v[76:79]
	v_mfma_f32_16x16x32_f16 v[80:83], v[182:185], v[166:169], v[80:83]
	v_mfma_f32_16x16x32_f16 v[84:87], v[190:193], v[166:169], v[84:87]
	v_mfma_f32_16x16x32_f16 v[88:91], v[182:185], v[174:177], v[88:91]
	v_mfma_f32_16x16x32_f16 v[92:95], v[190:193], v[174:177], v[92:95]
	s_setprio 0
	s_addk_i32 s7, 0x100
	s_cmp_lt_u32 s8, 32
	s_mov_b32 s8, s9
	s_barrier
	s_cbranch_scc1 .LBB1_82
	ds_read_b128 v[132:135], v219 offset:32768
	ds_read_b128 v[136:139], v219 offset:33792
	ds_read_b128 v[140:143], v219 offset:34816
	ds_read_b128 v[144:147], v219 offset:35840
	ds_read_b128 v[128:131], v220
	ds_read_b128 v[148:151], v220 offset:1024
	ds_read_b128 v[152:155], v221
	ds_read_b128 v[156:159], v221 offset:1024
	ds_read_b128 v[188:191], v222
	ds_read_b128 v[192:195], v222 offset:1024
	ds_read_b128 v[196:199], v223
	ds_read_b128 v[200:203], v223 offset:1024
	s_setprio 2
	s_lshl_b32 s3, s50, 9
	s_add_i32 s3, s47, s3
	s_add_i32 s3, s3, 0x10380
	s_mov_b32 m0, s43
	v_add_u32_e32 v160, s3, v206
	global_load_lds_dwordx4 v160, s[18:19]
	v_add_u32_e32 v160, s3, v213
	s_mov_b32 m0, s44
	s_nop 0
	global_load_lds_dwordx4 v160, s[18:19]
	s_setprio 0
	s_waitcnt vmcnt(8)
	s_waitcnt lgkmcnt(0)
	s_barrier
	s_waitcnt lgkmcnt(0)
	s_setprio 1
	s_waitcnt lgkmcnt(0)
	v_mfma_f32_16x16x32_f16 v[124:127], v[132:135], v[128:131], v[124:127]
	v_mfma_f32_16x16x32_f16 v[120:123], v[140:143], v[128:131], v[120:123]
	v_mfma_f32_16x16x32_f16 v[116:119], v[132:135], v[152:155], v[116:119]
	v_mfma_f32_16x16x32_f16 v[112:115], v[140:143], v[152:155], v[112:115]
	v_mfma_f32_16x16x32_f16 v[108:111], v[132:135], v[188:191], v[108:111]
	v_mfma_f32_16x16x32_f16 v[104:107], v[140:143], v[188:191], v[104:107]
	v_mfma_f32_16x16x32_f16 v[100:103], v[132:135], v[196:199], v[100:103]
	v_mfma_f32_16x16x32_f16 v[96:99], v[140:143], v[196:199], v[96:99]
	v_mfma_f32_16x16x32_f16 v[160:163], v[136:139], v[148:151], v[124:127]
	v_mfma_f32_16x16x32_f16 v[164:167], v[144:147], v[148:151], v[120:123]
	v_mfma_f32_16x16x32_f16 v[168:171], v[136:139], v[156:159], v[116:119]
	v_mfma_f32_16x16x32_f16 v[172:175], v[144:147], v[156:159], v[112:115]
	v_mfma_f32_16x16x32_f16 v[176:179], v[136:139], v[192:195], v[108:111]
	v_mfma_f32_16x16x32_f16 v[180:183], v[144:147], v[192:195], v[104:107]
	v_mfma_f32_16x16x32_f16 v[100:103], v[136:139], v[200:203], v[100:103]
	v_mfma_f32_16x16x32_f16 v[184:187], v[144:147], v[200:203], v[96:99]
	s_setprio 0
	s_barrier
	ds_read_b128 v[104:107], v219 offset:49152
	ds_read_b128 v[108:111], v219 offset:50176
	ds_read_b128 v[116:119], v219 offset:51200
	ds_read_b128 v[236:239], v219 offset:52224
	s_waitcnt lgkmcnt(0)
	s_barrier
	s_waitcnt lgkmcnt(0)
	s_setprio 1
	s_waitcnt lgkmcnt(0)
	v_mfma_f32_16x16x32_f16 v[52:55], v[104:107], v[128:131], v[52:55]
	v_mfma_f32_16x16x32_f16 v[40:43], v[116:119], v[128:131], v[40:43]
	v_mfma_f32_16x16x32_f16 v[36:39], v[104:107], v[152:155], v[36:39]
	v_mfma_f32_16x16x32_f16 v[32:35], v[116:119], v[152:155], v[32:35]
	v_mfma_f32_16x16x32_f16 v[28:31], v[104:107], v[188:191], v[28:31]
	v_mfma_f32_16x16x32_f16 v[24:27], v[116:119], v[188:191], v[24:27]
	v_mfma_f32_16x16x32_f16 v[20:23], v[104:107], v[196:199], v[20:23]
	v_mfma_f32_16x16x32_f16 v[16:19], v[116:119], v[196:199], v[16:19]
	v_mfma_f32_16x16x32_f16 v[52:55], v[108:111], v[148:151], v[52:55]
	v_mfma_f32_16x16x32_f16 v[40:43], v[236:239], v[148:151], v[40:43]
	v_mfma_f32_16x16x32_f16 v[36:39], v[108:111], v[156:159], v[36:39]
	v_mfma_f32_16x16x32_f16 v[32:35], v[236:239], v[156:159], v[32:35]
	v_mfma_f32_16x16x32_f16 v[28:31], v[108:111], v[192:195], v[28:31]
	v_mfma_f32_16x16x32_f16 v[24:27], v[236:239], v[192:195], v[24:27]
	v_mfma_f32_16x16x32_f16 v[96:99], v[108:111], v[200:203], v[20:23]
	v_mfma_f32_16x16x32_f16 v[16:19], v[236:239], v[200:203], v[16:19]
	s_setprio 0
	s_barrier
	ds_read_b128 v[20:23], v220 offset:16384
	ds_read_b128 v[148:151], v220 offset:17408
	ds_read_b128 v[152:155], v221 offset:16384
	ds_read_b128 v[156:159], v221 offset:17408
	ds_read_b128 v[188:191], v222 offset:16384
	ds_read_b128 v[192:195], v222 offset:17408
	ds_read_b128 v[196:199], v223 offset:16384
	ds_read_b128 v[200:203], v223 offset:17408
	s_waitcnt vmcnt(4)
	s_waitcnt lgkmcnt(0)
	s_barrier
	s_waitcnt lgkmcnt(0)
	s_setprio 1
	s_waitcnt lgkmcnt(0)
	v_mfma_f32_16x16x32_f16 v[0:3], v[140:143], v[152:155], v[0:3]
	v_mfma_f32_16x16x32_f16 v[124:127], v[144:147], v[156:159], v[0:3]
	v_mfma_f32_16x16x32_f16 v[0:3], v[132:135], v[188:191], v[44:47]
	v_mfma_f32_16x16x32_f16 v[128:131], v[136:139], v[192:195], v[0:3]
	v_mfma_f32_16x16x32_f16 v[0:3], v[140:143], v[188:191], v[48:51]
	v_mfma_f32_16x16x32_f16 v[48:51], v[144:147], v[192:195], v[0:3]
	v_mfma_f32_16x16x32_f16 v[0:3], v[132:135], v[196:199], v[56:59]
	v_mfma_f32_16x16x32_f16 v[12:15], v[132:135], v[20:23], v[12:15]
	v_mfma_f32_16x16x32_f16 v[8:11], v[140:143], v[20:23], v[8:11]
	v_mfma_f32_16x16x32_f16 v[4:7], v[132:135], v[152:155], v[4:7]
	v_mfma_f32_16x16x32_f16 v[56:59], v[136:139], v[200:203], v[0:3]
	v_mfma_f32_16x16x32_f16 v[0:3], v[140:143], v[196:199], v[60:63]
	v_mfma_f32_16x16x32_f16 v[112:115], v[136:139], v[148:151], v[12:15]
	v_mfma_f32_16x16x32_f16 v[8:11], v[144:147], v[148:151], v[8:11]
	v_mfma_f32_16x16x32_f16 v[120:123], v[136:139], v[156:159], v[4:7]
	v_mfma_f32_16x16x32_f16 v[60:63], v[144:147], v[200:203], v[0:3]
	s_setprio 0
	s_setprio 1
	v_mfma_f32_16x16x32_f16 v[0:3], v[104:107], v[20:23], v[64:67]
	v_mfma_f32_16x16x32_f16 v[132:135], v[108:111], v[148:151], v[0:3]
	v_mfma_f32_16x16x32_f16 v[0:3], v[116:119], v[20:23], v[68:71]
	v_mfma_f32_16x16x32_f16 v[136:139], v[236:239], v[148:151], v[0:3]
	v_mfma_f32_16x16x32_f16 v[0:3], v[104:107], v[152:155], v[72:75]
	v_mfma_f32_16x16x32_f16 v[140:143], v[108:111], v[156:159], v[0:3]
	v_mfma_f32_16x16x32_f16 v[0:3], v[116:119], v[152:155], v[76:79]
	v_mfma_f32_16x16x32_f16 v[144:147], v[236:239], v[156:159], v[0:3]
	v_mfma_f32_16x16x32_f16 v[0:3], v[104:107], v[188:191], v[80:83]
	v_mfma_f32_16x16x32_f16 v[80:83], v[108:111], v[192:195], v[0:3]
	v_mfma_f32_16x16x32_f16 v[0:3], v[116:119], v[188:191], v[84:87]
	v_mfma_f32_16x16x32_f16 v[148:151], v[236:239], v[192:195], v[0:3]
	v_mfma_f32_16x16x32_f16 v[0:3], v[104:107], v[196:199], v[88:91]
	v_mfma_f32_16x16x32_f16 v[152:155], v[108:111], v[200:203], v[0:3]
	v_mfma_f32_16x16x32_f16 v[0:3], v[116:119], v[196:199], v[92:95]
	v_mfma_f32_16x16x32_f16 v[156:159], v[236:239], v[200:203], v[0:3]
	s_setprio 0
	s_add_i32 s49, s49, s17
	s_cmpk_lt_i32 s49, 0x1c8
	s_cselect_b64 s[6:7], -1, 0
	s_cmpk_gt_i32 s49, 0x1c7
	s_cselect_b64 s[12:13], -1, 0
	s_and_b64 vcc, exec, s[12:13]
	s_mov_b32 s54, s2
	s_mov_b32 s53, s51
	s_mov_b32 s55, s52
	s_barrier
	s_cbranch_vccnz .LBB1_100
	s_cmpk_lt_i32 s49, 0x148
	s_cbranch_scc1 .LBB1_88
	s_cmpk_lt_u32 s49, 0x1a0
	s_cbranch_scc1 .LBB1_89
	s_cmpk_lt_u32 s49, 0x1b8
	s_cbranch_scc1 .LBB1_90
	s_cmpk_lt_u32 s49, 0x1c0
	s_cselect_b32 s47, s45, 0xfffffe40
	s_cselect_b32 s48, 3, 4
	s_mov_b32 s3, 1
	s_cmp_lt_i32 s48, 1
	s_movk_i32 s53, 0x64
	s_cbranch_scc0 .LBB1_91
	s_branch .LBB1_99

.LBB1_100:
	ds_read_b128 v[84:87], v224
	ds_read_b128 v[188:191], v224 offset:1024
	ds_read_b128 v[192:195], v224 offset:2048
	ds_read_b128 v[196:199], v224 offset:3072
	ds_read_b128 v[20:23], v225
	ds_read_b128 v[44:47], v225 offset:1024
	ds_read_b128 v[12:15], v226
	ds_read_b128 v[200:203], v226 offset:1024
	ds_read_b128 v[4:7], v227
	ds_read_b128 v[92:95], v227 offset:1024
	ds_read_b128 v[0:3], v228
	ds_read_b128 v[88:91], v228 offset:1024
	s_waitcnt vmcnt(2)
	s_andn2_b64 vcc, exec, s[6:7]
	s_waitcnt lgkmcnt(0)
	s_barrier
	s_cbranch_vccnz .LBB1_102
	s_setprio 2
	s_mov_b32 m0, s22
	v_add_u32_e32 v64, s48, v207
	global_load_lds_dwordx4 v64, s[10:11]
	v_add_u32_e32 v64, s48, v208
	s_mov_b32 m0, s23
	s_nop 0
	global_load_lds_dwordx4 v64, s[10:11]
	s_setprio 0
	s_setprio 2
	s_not_b32 s3, s50
	s_lshl_b32 s3, s3, 9
	s_add_i32 s3, s3, s47
	s_mov_b32 m0, s21
	v_add_u32_e32 v64, s3, v206
	global_load_lds_dwordx4 v64, s[18:19]
	v_add_u32_e32 v64, s3, v213
	s_mov_b32 m0, s24
	s_nop 0
	global_load_lds_dwordx4 v64, s[18:19]
	s_setprio 0
	s_setprio 2
	s_mov_b32 m0, s25
	v_add_u32_e32 v64, s48, v209
	global_load_lds_dwordx4 v64, s[10:11]
	v_add_u32_e32 v64, s48, v210
	s_mov_b32 m0, s26
	s_nop 0
	global_load_lds_dwordx4 v64, s[10:11]
	s_setprio 0
	s_setprio 2
	s_lshl_b32 s3, s50, 9
	s_sub_i32 s3, s47, s3
	s_mov_b32 m0, s27
	v_add_u32_e32 v64, s3, v216
	global_load_lds_dwordx4 v64, s[18:19]
	v_add_u32_e32 v64, s3, v217
	s_mov_b32 m0, s28
	s_nop 0
	global_load_lds_dwordx4 v64, s[18:19]
	s_setprio 0

.LBB1_106:
	s_waitcnt lgkmcnt(0)
	s_barrier
	s_waitcnt lgkmcnt(0)
	s_setprio 1
	s_waitcnt lgkmcnt(0)
	v_mfma_f32_16x16x32_f16 v[52:55], v[168:171], v[20:23], v[52:55]
	v_mfma_f32_16x16x32_f16 v[20:23], v[176:179], v[20:23], v[40:43]
	v_mfma_f32_16x16x32_f16 v[36:39], v[168:171], v[12:15], v[36:39]
	v_mfma_f32_16x16x32_f16 v[12:15], v[176:179], v[12:15], v[32:35]
	v_mfma_f32_16x16x32_f16 v[28:31], v[168:171], v[4:7], v[28:31]
	v_mfma_f32_16x16x32_f16 v[4:7], v[176:179], v[4:7], v[24:27]
	v_mfma_f32_16x16x32_f16 v[24:27], v[168:171], v[0:3], v[96:99]
	v_mfma_f32_16x16x32_f16 v[0:3], v[176:179], v[0:3], v[16:19]
	v_mfma_f32_16x16x32_f16 v[52:55], v[172:175], v[44:47], v[52:55]
	v_mfma_f32_16x16x32_f16 v[20:23], v[180:183], v[44:47], v[20:23]
	v_mfma_f32_16x16x32_f16 v[44:47], v[172:175], v[200:203], v[36:39]
	v_mfma_f32_16x16x32_f16 v[12:15], v[180:183], v[200:203], v[12:15]
	v_mfma_f32_16x16x32_f16 v[36:39], v[172:175], v[92:95], v[28:31]
	v_mfma_f32_16x16x32_f16 v[4:7], v[180:183], v[92:95], v[4:7]
	v_mfma_f32_16x16x32_f16 v[32:35], v[172:175], v[88:91], v[24:27]
	v_mfma_f32_16x16x32_f16 v[0:3], v[180:183], v[88:91], v[0:3]
	s_setprio 0
	s_barrier
	ds_read_b128 v[16:19], v230
	ds_read_b128 v[24:27], v230 offset:1024
	ds_read_b128 v[40:43], v231
	ds_read_b128 v[184:187], v231 offset:1024
	ds_read_b128 v[200:203], v232
	ds_read_b128 v[236:239], v232 offset:1024
	ds_read_b128 v[240:243], v233
	ds_read_b128 v[244:247], v233 offset:1024
	s_waitcnt lgkmcnt(0)
	s_barrier
	s_waitcnt lgkmcnt(0)
	s_setprio 1
	s_waitcnt lgkmcnt(0)
	v_mfma_f32_16x16x32_f16 v[8:11], v[192:195], v[16:19], v[8:11]
	v_mfma_f32_16x16x32_f16 v[96:99], v[196:199], v[24:27], v[8:11]
	v_mfma_f32_16x16x32_f16 v[8:11], v[84:87], v[40:43], v[120:123]
	v_mfma_f32_16x16x32_f16 v[160:163], v[188:191], v[184:187], v[8:11]
	v_mfma_f32_16x16x32_f16 v[8:11], v[192:195], v[40:43], v[124:127]
	v_mfma_f32_16x16x32_f16 v[92:95], v[196:199], v[184:187], v[8:11]
	v_mfma_f32_16x16x32_f16 v[8:11], v[84:87], v[200:203], v[128:131]
	v_mfma_f32_16x16x32_f16 v[124:127], v[188:191], v[236:239], v[8:11]
	v_mfma_f32_16x16x32_f16 v[8:11], v[192:195], v[200:203], v[48:51]
	v_mfma_f32_16x16x32_f16 v[88:91], v[196:199], v[236:239], v[8:11]
	v_mfma_f32_16x16x32_f16 v[8:11], v[84:87], v[240:243], v[56:59]
	v_mfma_f32_16x16x32_f16 v[28:31], v[84:87], v[16:19], v[112:115]
	v_mfma_f32_16x16x32_f16 v[120:123], v[188:191], v[244:247], v[8:11]
	v_mfma_f32_16x16x32_f16 v[8:11], v[192:195], v[240:243], v[60:63]
	v_mfma_f32_16x16x32_f16 v[164:167], v[188:191], v[24:27], v[28:31]
	v_mfma_f32_16x16x32_f16 v[84:87], v[196:199], v[244:247], v[8:11]
	s_setprio 0
	s_setprio 1
	v_mfma_f32_16x16x32_f16 v[8:11], v[168:171], v[16:19], v[132:135]
	v_mfma_f32_16x16x32_f16 v[60:63], v[172:175], v[24:27], v[8:11]
	v_mfma_f32_16x16x32_f16 v[8:11], v[176:179], v[16:19], v[136:139]
	v_mfma_f32_16x16x32_f16 v[28:31], v[180:183], v[24:27], v[8:11]
	v_mfma_f32_16x16x32_f16 v[8:11], v[168:171], v[40:43], v[140:143]
	v_mfma_f32_16x16x32_f16 v[56:59], v[172:175], v[184:187], v[8:11]
	v_mfma_f32_16x16x32_f16 v[8:11], v[176:179], v[40:43], v[144:147]
	v_mfma_f32_16x16x32_f16 v[24:27], v[180:183], v[184:187], v[8:11]
	v_mfma_f32_16x16x32_f16 v[8:11], v[168:171], v[200:203], v[80:83]
	v_mfma_f32_16x16x32_f16 v[48:51], v[172:175], v[236:239], v[8:11]
	v_mfma_f32_16x16x32_f16 v[8:11], v[176:179], v[200:203], v[148:151]
	v_mfma_f32_16x16x32_f16 v[16:19], v[180:183], v[236:239], v[8:11]
	v_mfma_f32_16x16x32_f16 v[8:11], v[168:171], v[240:243], v[152:155]
	v_mfma_f32_16x16x32_f16 v[40:43], v[172:175], v[244:247], v[8:11]
	v_mfma_f32_16x16x32_f16 v[8:11], v[176:179], v[240:243], v[156:159]
	v_mfma_f32_16x16x32_f16 v[8:11], v[180:183], v[244:247], v[8:11]
	s_setprio 0
	s_barrier
	s_and_saveexec_b64 s[6:7], s[0:1]
	s_cbranch_execz .LBB1_108
	s_barrier
